# speedup vs baseline: 1.0103x; 1.0103x over previous
.Lc0_back0:
	v_pk_fma_f16 v6, v2, v138, v139 op_sel:[0,0,0] op_sel_hi:[1,0,0] neg_lo:[1,0,0] neg_hi:[1,0,0]
	v_pk_fma_f16 v7, v3, v138, v139 op_sel:[0,0,0] op_sel_hi:[1,0,0] neg_lo:[1,0,0] neg_hi:[1,0,0]
	v_pk_fma_f16 v8, v4, v138, v139 op_sel:[0,0,0] op_sel_hi:[1,0,0] neg_lo:[1,0,0] neg_hi:[1,0,0]
	v_pk_fma_f16 v9, v5, v138, v139 op_sel:[0,0,0] op_sel_hi:[1,0,0] neg_lo:[1,0,0] neg_hi:[1,0,0]
	v_mfma_f32_16x16x32_f16 v[22:25], v[10:13], v[2:5], 0
	ds_read2_b64 v[108:111], v32 offset0:15 offset1:217
	v_pk_fma_f16 v2, v84, v6, v2
	v_pk_fma_f16 v3, v85, v7, v3
	v_pk_fma_f16 v4, v86, v8, v4
	v_pk_fma_f16 v5, v87, v9, v5
	v_cndmask_b32_e64 v26, v26, v18, s[64:65]
	s_waitcnt lgkmcnt(6)
	v_pk_fma_f16 v6, v2, v140, v141 op_sel:[0,0,0] op_sel_hi:[1,0,0] neg_lo:[1,0,0] neg_hi:[1,0,0]
	v_pk_fma_f16 v7, v3, v140, v141 op_sel:[0,0,0] op_sel_hi:[1,0,0] neg_lo:[1,0,0] neg_hi:[1,0,0]
	v_pk_fma_f16 v8, v4, v140, v141 op_sel:[0,0,0] op_sel_hi:[1,0,0] neg_lo:[1,0,0] neg_hi:[1,0,0]
	v_pk_fma_f16 v9, v5, v140, v141 op_sel:[0,0,0] op_sel_hi:[1,0,0] neg_lo:[1,0,0] neg_hi:[1,0,0]
	v_mfma_f32_16x16x32_f16 v[18:21], v[10:13], v[2:5], 0
	ds_read2_b64 v[48:51], v32 offset0:16 offset1:218
	ds_read_b128 v[120:123], v33 offset:128
	ds_read2_b64 v[14:17], v34 offset0:16 offset1:218
	v_pk_fma_f16 v2, v88, v6, v2
	v_pk_fma_f16 v3, v89, v7, v3
	v_pk_fma_f16 v4, v90, v8, v4
	v_pk_fma_f16 v5, v91, v9, v5
	v_cndmask_b32_e64 v27, v27, v23, s[64:65]
	v_pk_fma_f16 v6, v2, v142, v143 op_sel:[0,0,0] op_sel_hi:[1,0,0] neg_lo:[1,0,0] neg_hi:[1,0,0]
	v_pk_fma_f16 v7, v3, v142, v143 op_sel:[0,0,0] op_sel_hi:[1,0,0] neg_lo:[1,0,0] neg_hi:[1,0,0]
	v_pk_fma_f16 v8, v4, v142, v143 op_sel:[0,0,0] op_sel_hi:[1,0,0] neg_lo:[1,0,0] neg_hi:[1,0,0]
	v_pk_fma_f16 v9, v5, v142, v143 op_sel:[0,0,0] op_sel_hi:[1,0,0] neg_lo:[1,0,0] neg_hi:[1,0,0]
	v_mfma_f32_16x16x32_f16 v[22:25], v[10:13], v[2:5], 0
	ds_read2_b64 v[52:55], v32 offset0:17 offset1:219
	v_pk_fma_f16 v2, v92, v6, v2
	v_pk_fma_f16 v3, v93, v7, v3
	v_pk_fma_f16 v4, v94, v8, v4
	v_pk_fma_f16 v5, v95, v9, v5
	v_cndmask_b32_e64 v28, v28, v20, s[64:65]
	s_waitcnt lgkmcnt(7)
	v_pk_fma_f16 v6, v2, v144, v145 op_sel:[0,0,0] op_sel_hi:[1,0,0] neg_lo:[1,0,0] neg_hi:[1,0,0]
	v_pk_fma_f16 v7, v3, v144, v145 op_sel:[0,0,0] op_sel_hi:[1,0,0] neg_lo:[1,0,0] neg_hi:[1,0,0]
	v_pk_fma_f16 v8, v4, v144, v145 op_sel:[0,0,0] op_sel_hi:[1,0,0] neg_lo:[1,0,0] neg_hi:[1,0,0]
	v_pk_fma_f16 v9, v5, v144, v145 op_sel:[0,0,0] op_sel_hi:[1,0,0] neg_lo:[1,0,0] neg_hi:[1,0,0]
	v_mfma_f32_16x16x32_f16 v[18:21], v[10:13], v[2:5], 0
	ds_read2_b64 v[56:59], v32 offset0:18 offset1:220
	ds_read_b128 v[124:127], v33 offset:144
	v_pk_fma_f16 v2, v96, v6, v2
	v_pk_fma_f16 v3, v97, v7, v3
	v_pk_fma_f16 v4, v98, v8, v4
	v_pk_fma_f16 v5, v99, v9, v5
	v_cndmask_b32_e64 v29, v29, v25, s[64:65]
	v_pk_fma_f16 v6, v2, v146, v147 op_sel:[0,0,0] op_sel_hi:[1,0,0] neg_lo:[1,0,0] neg_hi:[1,0,0]
	v_pk_fma_f16 v7, v3, v146, v147 op_sel:[0,0,0] op_sel_hi:[1,0,0] neg_lo:[1,0,0] neg_hi:[1,0,0]
	v_pk_fma_f16 v8, v4, v146, v147 op_sel:[0,0,0] op_sel_hi:[1,0,0] neg_lo:[1,0,0] neg_hi:[1,0,0]
	v_pk_fma_f16 v9, v5, v146, v147 op_sel:[0,0,0] op_sel_hi:[1,0,0] neg_lo:[1,0,0] neg_hi:[1,0,0]
	v_mfma_f32_16x16x32_f16 v[22:25], v[10:13], v[2:5], 0
	ds_read2_b64 v[60:63], v32 offset0:19 offset1:221
	v_pk_fma_f16 v2, v100, v6, v2
	v_pk_fma_f16 v3, v101, v7, v3
	v_pk_fma_f16 v4, v102, v8, v4
	v_pk_fma_f16 v5, v103, v9, v5
	v_cndmask_b32_e64 v26, v26, v18, s[66:67]
	s_waitcnt lgkmcnt(7)
	v_pk_fma_f16 v6, v2, v148, v149 op_sel:[0,0,0] op_sel_hi:[1,0,0] neg_lo:[1,0,0] neg_hi:[1,0,0]
	v_pk_fma_f16 v7, v3, v148, v149 op_sel:[0,0,0] op_sel_hi:[1,0,0] neg_lo:[1,0,0] neg_hi:[1,0,0]
	v_pk_fma_f16 v8, v4, v148, v149 op_sel:[0,0,0] op_sel_hi:[1,0,0] neg_lo:[1,0,0] neg_hi:[1,0,0]
	v_pk_fma_f16 v9, v5, v148, v149 op_sel:[0,0,0] op_sel_hi:[1,0,0] neg_lo:[1,0,0] neg_hi:[1,0,0]
	v_mfma_f32_16x16x32_f16 v[18:21], v[10:13], v[2:5], 0
	ds_read2_b64 v[64:67], v32 offset0:20 offset1:222
	ds_read_b128 v[128:131], v33 offset:160
	v_pk_fma_f16 v2, v104, v6, v2
	v_pk_fma_f16 v3, v105, v7, v3
	v_pk_fma_f16 v4, v106, v8, v4
	v_pk_fma_f16 v5, v107, v9, v5
	v_cndmask_b32_e64 v27, v27, v23, s[66:67]
	v_pk_fma_f16 v6, v2, v150, v151 op_sel:[0,0,0] op_sel_hi:[1,0,0] neg_lo:[1,0,0] neg_hi:[1,0,0]
	v_pk_fma_f16 v7, v3, v150, v151 op_sel:[0,0,0] op_sel_hi:[1,0,0] neg_lo:[1,0,0] neg_hi:[1,0,0]
	v_pk_fma_f16 v8, v4, v150, v151 op_sel:[0,0,0] op_sel_hi:[1,0,0] neg_lo:[1,0,0] neg_hi:[1,0,0]
	v_pk_fma_f16 v9, v5, v150, v151 op_sel:[0,0,0] op_sel_hi:[1,0,0] neg_lo:[1,0,0] neg_hi:[1,0,0]
	v_mfma_f32_16x16x32_f16 v[22:25], v[10:13], v[2:5], 0
	ds_read2_b64 v[68:71], v32 offset0:21 offset1:223
	v_pk_fma_f16 v2, v108, v6, v2
	v_pk_fma_f16 v3, v109, v7, v3
	v_pk_fma_f16 v4, v110, v8, v4
	v_pk_fma_f16 v5, v111, v9, v5
	v_cndmask_b32_e64 v28, v28, v20, s[66:67]

.Lc0_back1:
	v_pk_fma_f16 v6, v2, v138, v139 op_sel:[0,0,0] op_sel_hi:[1,0,0] neg_lo:[1,0,0] neg_hi:[1,0,0]
	v_pk_fma_f16 v7, v3, v138, v139 op_sel:[0,0,0] op_sel_hi:[1,0,0] neg_lo:[1,0,0] neg_hi:[1,0,0]
	v_pk_fma_f16 v8, v4, v138, v139 op_sel:[0,0,0] op_sel_hi:[1,0,0] neg_lo:[1,0,0] neg_hi:[1,0,0]
	v_pk_fma_f16 v9, v5, v138, v139 op_sel:[0,0,0] op_sel_hi:[1,0,0] neg_lo:[1,0,0] neg_hi:[1,0,0]
	v_mfma_f32_16x16x32_f16 v[22:25], v[14:17], v[2:5], 0
	ds_read2_b64 v[108:111], v32 offset0:31 offset1:233
	v_pk_fma_f16 v2, v84, v6, v2
	v_pk_fma_f16 v3, v85, v7, v3
	v_pk_fma_f16 v4, v86, v8, v4
	v_pk_fma_f16 v5, v87, v9, v5
	v_cndmask_b32_e64 v26, v26, v18, s[64:65]
	s_waitcnt lgkmcnt(6)
	v_pk_fma_f16 v6, v2, v140, v141 op_sel:[0,0,0] op_sel_hi:[1,0,0] neg_lo:[1,0,0] neg_hi:[1,0,0]
	v_pk_fma_f16 v7, v3, v140, v141 op_sel:[0,0,0] op_sel_hi:[1,0,0] neg_lo:[1,0,0] neg_hi:[1,0,0]
	v_pk_fma_f16 v8, v4, v140, v141 op_sel:[0,0,0] op_sel_hi:[1,0,0] neg_lo:[1,0,0] neg_hi:[1,0,0]
	v_pk_fma_f16 v9, v5, v140, v141 op_sel:[0,0,0] op_sel_hi:[1,0,0] neg_lo:[1,0,0] neg_hi:[1,0,0]
	v_mfma_f32_16x16x32_f16 v[18:21], v[14:17], v[2:5], 0
	ds_read2_b64 v[48:51], v32 offset0:32 offset1:234
	ds_read_b128 v[120:123], v33 offset:256
	ds_read2_b64 v[10:13], v34 offset0:32 offset1:234
	v_pk_fma_f16 v2, v88, v6, v2
	v_pk_fma_f16 v3, v89, v7, v3
	v_pk_fma_f16 v4, v90, v8, v4
	v_pk_fma_f16 v5, v91, v9, v5
	v_cndmask_b32_e64 v27, v27, v23, s[64:65]
	v_pk_fma_f16 v6, v2, v142, v143 op_sel:[0,0,0] op_sel_hi:[1,0,0] neg_lo:[1,0,0] neg_hi:[1,0,0]
	v_pk_fma_f16 v7, v3, v142, v143 op_sel:[0,0,0] op_sel_hi:[1,0,0] neg_lo:[1,0,0] neg_hi:[1,0,0]
	v_pk_fma_f16 v8, v4, v142, v143 op_sel:[0,0,0] op_sel_hi:[1,0,0] neg_lo:[1,0,0] neg_hi:[1,0,0]
	v_pk_fma_f16 v9, v5, v142, v143 op_sel:[0,0,0] op_sel_hi:[1,0,0] neg_lo:[1,0,0] neg_hi:[1,0,0]
	v_mfma_f32_16x16x32_f16 v[22:25], v[14:17], v[2:5], 0
	ds_read2_b64 v[52:55], v32 offset0:33 offset1:235
	v_pk_fma_f16 v2, v92, v6, v2
	v_pk_fma_f16 v3, v93, v7, v3
	v_pk_fma_f16 v4, v94, v8, v4
	v_pk_fma_f16 v5, v95, v9, v5
	v_cndmask_b32_e64 v28, v28, v20, s[64:65]
	s_waitcnt lgkmcnt(7)
	v_pk_fma_f16 v6, v2, v144, v145 op_sel:[0,0,0] op_sel_hi:[1,0,0] neg_lo:[1,0,0] neg_hi:[1,0,0]
	v_pk_fma_f16 v7, v3, v144, v145 op_sel:[0,0,0] op_sel_hi:[1,0,0] neg_lo:[1,0,0] neg_hi:[1,0,0]
	v_pk_fma_f16 v8, v4, v144, v145 op_sel:[0,0,0] op_sel_hi:[1,0,0] neg_lo:[1,0,0] neg_hi:[1,0,0]
	v_pk_fma_f16 v9, v5, v144, v145 op_sel:[0,0,0] op_sel_hi:[1,0,0] neg_lo:[1,0,0] neg_hi:[1,0,0]
	v_mfma_f32_16x16x32_f16 v[18:21], v[14:17], v[2:5], 0
	ds_read2_b64 v[56:59], v32 offset0:34 offset1:236
	ds_read_b128 v[124:127], v33 offset:272
	v_pk_fma_f16 v2, v96, v6, v2
	v_pk_fma_f16 v3, v97, v7, v3
	v_pk_fma_f16 v4, v98, v8, v4
	v_pk_fma_f16 v5, v99, v9, v5
	v_cndmask_b32_e64 v29, v29, v25, s[64:65]
	v_pk_fma_f16 v6, v2, v146, v147 op_sel:[0,0,0] op_sel_hi:[1,0,0] neg_lo:[1,0,0] neg_hi:[1,0,0]
	v_pk_fma_f16 v7, v3, v146, v147 op_sel:[0,0,0] op_sel_hi:[1,0,0] neg_lo:[1,0,0] neg_hi:[1,0,0]
	v_pk_fma_f16 v8, v4, v146, v147 op_sel:[0,0,0] op_sel_hi:[1,0,0] neg_lo:[1,0,0] neg_hi:[1,0,0]
	v_pk_fma_f16 v9, v5, v146, v147 op_sel:[0,0,0] op_sel_hi:[1,0,0] neg_lo:[1,0,0] neg_hi:[1,0,0]
	v_mfma_f32_16x16x32_f16 v[22:25], v[14:17], v[2:5], 0
	ds_read2_b64 v[60:63], v32 offset0:35 offset1:237
	v_pk_fma_f16 v2, v100, v6, v2
	v_pk_fma_f16 v3, v101, v7, v3
	v_pk_fma_f16 v4, v102, v8, v4
	v_pk_fma_f16 v5, v103, v9, v5
	v_cndmask_b32_e64 v26, v26, v18, s[66:67]
	s_waitcnt lgkmcnt(7)
	v_pk_fma_f16 v6, v2, v148, v149 op_sel:[0,0,0] op_sel_hi:[1,0,0] neg_lo:[1,0,0] neg_hi:[1,0,0]
	v_pk_fma_f16 v7, v3, v148, v149 op_sel:[0,0,0] op_sel_hi:[1,0,0] neg_lo:[1,0,0] neg_hi:[1,0,0]
	v_pk_fma_f16 v8, v4, v148, v149 op_sel:[0,0,0] op_sel_hi:[1,0,0] neg_lo:[1,0,0] neg_hi:[1,0,0]
	v_pk_fma_f16 v9, v5, v148, v149 op_sel:[0,0,0] op_sel_hi:[1,0,0] neg_lo:[1,0,0] neg_hi:[1,0,0]
	v_mfma_f32_16x16x32_f16 v[18:21], v[14:17], v[2:5], 0
	ds_read2_b64 v[64:67], v32 offset0:36 offset1:238
	ds_read_b128 v[128:131], v33 offset:288
	v_pk_fma_f16 v2, v104, v6, v2
	v_pk_fma_f16 v3, v105, v7, v3
	v_pk_fma_f16 v4, v106, v8, v4
	v_pk_fma_f16 v5, v107, v9, v5
	v_cndmask_b32_e64 v27, v27, v23, s[66:67]
	v_pk_fma_f16 v6, v2, v150, v151 op_sel:[0,0,0] op_sel_hi:[1,0,0] neg_lo:[1,0,0] neg_hi:[1,0,0]
	v_pk_fma_f16 v7, v3, v150, v151 op_sel:[0,0,0] op_sel_hi:[1,0,0] neg_lo:[1,0,0] neg_hi:[1,0,0]
	v_pk_fma_f16 v8, v4, v150, v151 op_sel:[0,0,0] op_sel_hi:[1,0,0] neg_lo:[1,0,0] neg_hi:[1,0,0]
	v_pk_fma_f16 v9, v5, v150, v151 op_sel:[0,0,0] op_sel_hi:[1,0,0] neg_lo:[1,0,0] neg_hi:[1,0,0]
	v_mfma_f32_16x16x32_f16 v[22:25], v[14:17], v[2:5], 0
	ds_read2_b64 v[68:71], v32 offset0:37 offset1:239
	v_pk_fma_f16 v2, v108, v6, v2
	v_pk_fma_f16 v3, v109, v7, v3
	v_pk_fma_f16 v4, v110, v8, v4
	v_pk_fma_f16 v5, v111, v9, v5
	v_cndmask_b32_e64 v28, v28, v20, s[66:67]
.Lc0_next1:
	v_add_u32_e32 v32, 0x100, v32
	v_add_u32_e32 v33, 0x100, v33
	v_add_u32_e32 v34, 0x100, v34
	v_add_u32_e32 v36, 8, v36
	v_add_u32_e32 v39, 0x1000, v39
	v_add_u32_e32 v43, 0x1000, v43
	v_add_u32_e32 v35, 0x800, v35
	s_xor_b32 s71, s71, 2
	s_add_i32 s70, s70, 1
	s_cmp_lt_u32 s70, 6
	s_cbranch_scc1 .Lc0_loop
	s_waitcnt lgkmcnt(6)
	v_pk_fma_f16 v6, v2, v120, v121 op_sel:[0,0,0] op_sel_hi:[1,0,0] neg_lo:[1,0,0] neg_hi:[1,0,0]
	v_pk_fma_f16 v7, v3, v120, v121 op_sel:[0,0,0] op_sel_hi:[1,0,0] neg_lo:[1,0,0] neg_hi:[1,0,0]
	v_pk_fma_f16 v8, v4, v120, v121 op_sel:[0,0,0] op_sel_hi:[1,0,0] neg_lo:[1,0,0] neg_hi:[1,0,0]
	v_pk_fma_f16 v9, v5, v120, v121 op_sel:[0,0,0] op_sel_hi:[1,0,0] neg_lo:[1,0,0] neg_hi:[1,0,0]
	v_mfma_f32_16x16x32_f16 v[18:21], v[10:13], v[2:5], 0
	ds_read2_b64 v[72:75], v32 offset0:6 offset1:208
	ds_read_b128 v[132:135], v33 offset:48
	v_pk_fma_f16 v2, v48, v6, v2
	v_pk_fma_f16 v3, v49, v7, v3
	v_pk_fma_f16 v4, v50, v8, v4
	v_pk_fma_f16 v5, v51, v9, v5
	v_cndmask_b32_e64 v29, v29, v25, s[66:67]
	v_cvt_pk_f16_f32 v30, v26, v27
	v_cvt_pk_f16_f32 v31, v28, v29
	ds_write_b16 v39, v30 offset:0
	ds_write_b16_d16_hi v39, v30 offset:64
	ds_write_b16 v39, v31 offset:128
	ds_write_b16_d16_hi v39, v31 offset:192
	s_mov_b64 exec, 1
	ds_add_u32 v36, v44 offset:124
	s_mov_b64 exec, -1
	v_pk_fma_f16 v6, v2, v122, v123 op_sel:[0,0,0] op_sel_hi:[1,0,0] neg_lo:[1,0,0] neg_hi:[1,0,0]
	v_pk_fma_f16 v7, v3, v122, v123 op_sel:[0,0,0] op_sel_hi:[1,0,0] neg_lo:[1,0,0] neg_hi:[1,0,0]
	v_pk_fma_f16 v8, v4, v122, v123 op_sel:[0,0,0] op_sel_hi:[1,0,0] neg_lo:[1,0,0] neg_hi:[1,0,0]
	v_pk_fma_f16 v9, v5, v122, v123 op_sel:[0,0,0] op_sel_hi:[1,0,0] neg_lo:[1,0,0] neg_hi:[1,0,0]
	v_mfma_f32_16x16x32_f16 v[22:25], v[10:13], v[2:5], 0
	ds_read2_b64 v[76:79], v32 offset0:7 offset1:209
	v_pk_fma_f16 v2, v52, v6, v2
	v_pk_fma_f16 v3, v53, v7, v3
	v_pk_fma_f16 v4, v54, v8, v4
	v_pk_fma_f16 v5, v55, v9, v5
	v_cndmask_b32_e64 v26, v26, v18, s[60:61]
	s_waitcnt lgkmcnt(11)
	v_pk_fma_f16 v6, v2, v124, v125 op_sel:[0,0,0] op_sel_hi:[1,0,0] neg_lo:[1,0,0] neg_hi:[1,0,0]
	v_pk_fma_f16 v7, v3, v124, v125 op_sel:[0,0,0] op_sel_hi:[1,0,0] neg_lo:[1,0,0] neg_hi:[1,0,0]
	v_pk_fma_f16 v8, v4, v124, v125 op_sel:[0,0,0] op_sel_hi:[1,0,0] neg_lo:[1,0,0] neg_hi:[1,0,0]
	v_pk_fma_f16 v9, v5, v124, v125 op_sel:[0,0,0] op_sel_hi:[1,0,0] neg_lo:[1,0,0] neg_hi:[1,0,0]
	v_mfma_f32_16x16x32_f16 v[18:21], v[10:13], v[2:5], 0
	v_pk_fma_f16 v2, v56, v6, v2
	v_pk_fma_f16 v3, v57, v7, v3
	v_pk_fma_f16 v4, v58, v8, v4
	v_pk_fma_f16 v5, v59, v9, v5
	v_cndmask_b32_e64 v27, v27, v23, s[60:61]
	v_pk_fma_f16 v6, v2, v126, v127 op_sel:[0,0,0] op_sel_hi:[1,0,0] neg_lo:[1,0,0] neg_hi:[1,0,0]
	v_pk_fma_f16 v7, v3, v126, v127 op_sel:[0,0,0] op_sel_hi:[1,0,0] neg_lo:[1,0,0] neg_hi:[1,0,0]
	v_pk_fma_f16 v8, v4, v126, v127 op_sel:[0,0,0] op_sel_hi:[1,0,0] neg_lo:[1,0,0] neg_hi:[1,0,0]
	v_pk_fma_f16 v9, v5, v126, v127 op_sel:[0,0,0] op_sel_hi:[1,0,0] neg_lo:[1,0,0] neg_hi:[1,0,0]
	v_mfma_f32_16x16x32_f16 v[22:25], v[10:13], v[2:5], 0
	v_pk_fma_f16 v2, v60, v6, v2
	v_pk_fma_f16 v3, v61, v7, v3
	v_pk_fma_f16 v4, v62, v8, v4
	v_pk_fma_f16 v5, v63, v9, v5
	v_cndmask_b32_e64 v28, v28, v20, s[60:61]
	s_waitcnt lgkmcnt(8)
	v_pk_fma_f16 v6, v2, v128, v129 op_sel:[0,0,0] op_sel_hi:[1,0,0] neg_lo:[1,0,0] neg_hi:[1,0,0]
	v_pk_fma_f16 v7, v3, v128, v129 op_sel:[0,0,0] op_sel_hi:[1,0,0] neg_lo:[1,0,0] neg_hi:[1,0,0]
	v_pk_fma_f16 v8, v4, v128, v129 op_sel:[0,0,0] op_sel_hi:[1,0,0] neg_lo:[1,0,0] neg_hi:[1,0,0]
	v_pk_fma_f16 v9, v5, v128, v129 op_sel:[0,0,0] op_sel_hi:[1,0,0] neg_lo:[1,0,0] neg_hi:[1,0,0]
	v_mfma_f32_16x16x32_f16 v[18:21], v[10:13], v[2:5], 0
	v_pk_fma_f16 v2, v64, v6, v2
	v_pk_fma_f16 v3, v65, v7, v3
	v_pk_fma_f16 v4, v66, v8, v4
	v_pk_fma_f16 v5, v67, v9, v5
	v_cndmask_b32_e64 v29, v29, v25, s[60:61]
	v_pk_fma_f16 v6, v2, v130, v131 op_sel:[0,0,0] op_sel_hi:[1,0,0] neg_lo:[1,0,0] neg_hi:[1,0,0]
	v_pk_fma_f16 v7, v3, v130, v131 op_sel:[0,0,0] op_sel_hi:[1,0,0] neg_lo:[1,0,0] neg_hi:[1,0,0]
	v_pk_fma_f16 v8, v4, v130, v131 op_sel:[0,0,0] op_sel_hi:[1,0,0] neg_lo:[1,0,0] neg_hi:[1,0,0]
	v_pk_fma_f16 v9, v5, v130, v131 op_sel:[0,0,0] op_sel_hi:[1,0,0] neg_lo:[1,0,0] neg_hi:[1,0,0]
	v_mfma_f32_16x16x32_f16 v[22:25], v[10:13], v[2:5], 0
	v_pk_fma_f16 v2, v68, v6, v2
	v_pk_fma_f16 v3, v69, v7, v3
	v_pk_fma_f16 v4, v70, v8, v4
	v_pk_fma_f16 v5, v71, v9, v5
	v_cndmask_b32_e64 v26, v26, v18, s[62:63]
	s_waitcnt lgkmcnt(0)
	v_pk_fma_f16 v6, v2, v132, v133 op_sel:[0,0,0] op_sel_hi:[1,0,0] neg_lo:[1,0,0] neg_hi:[1,0,0]
	v_pk_fma_f16 v7, v3, v132, v133 op_sel:[0,0,0] op_sel_hi:[1,0,0] neg_lo:[1,0,0] neg_hi:[1,0,0]
	v_pk_fma_f16 v8, v4, v132, v133 op_sel:[0,0,0] op_sel_hi:[1,0,0] neg_lo:[1,0,0] neg_hi:[1,0,0]
	v_pk_fma_f16 v9, v5, v132, v133 op_sel:[0,0,0] op_sel_hi:[1,0,0] neg_lo:[1,0,0] neg_hi:[1,0,0]
	v_mfma_f32_16x16x32_f16 v[18:21], v[10:13], v[2:5], 0
	v_pk_fma_f16 v2, v72, v6, v2
	v_pk_fma_f16 v3, v73, v7, v3
	v_pk_fma_f16 v4, v74, v8, v4
	v_pk_fma_f16 v5, v75, v9, v5
	v_cndmask_b32_e64 v27, v27, v23, s[62:63]
	v_pk_fma_f16 v6, v2, v134, v135 op_sel:[0,0,0] op_sel_hi:[1,0,0] neg_lo:[1,0,0] neg_hi:[1,0,0]
	v_pk_fma_f16 v7, v3, v134, v135 op_sel:[0,0,0] op_sel_hi:[1,0,0] neg_lo:[1,0,0] neg_hi:[1,0,0]
	v_pk_fma_f16 v8, v4, v134, v135 op_sel:[0,0,0] op_sel_hi:[1,0,0] neg_lo:[1,0,0] neg_hi:[1,0,0]
	v_pk_fma_f16 v9, v5, v134, v135 op_sel:[0,0,0] op_sel_hi:[1,0,0] neg_lo:[1,0,0] neg_hi:[1,0,0]
	v_mfma_f32_16x16x32_f16 v[22:25], v[10:13], v[2:5], 0
	v_pk_fma_f16 v2, v76, v6, v2
	v_pk_fma_f16 v3, v77, v7, v3
	v_pk_fma_f16 v4, v78, v8, v4
	v_pk_fma_f16 v5, v79, v9, v5
	v_cndmask_b32_e64 v28, v28, v20, s[62:63]
	s_nop 7
	v_cndmask_b32_e64 v29, v29, v25, s[62:63]
	v_cvt_pk_f16_f32 v30, v26, v27
	v_cvt_pk_f16_f32 v31, v28, v29
	ds_write_b16 v39, v30 offset:2048
	ds_write_b16_d16_hi v39, v30 offset:2112
	ds_write_b16 v39, v31 offset:2176
	ds_write_b16_d16_hi v39, v31 offset:2240
	s_mov_b64 exec, 1
	ds_add_u32 v36, v44 offset:128
	s_mov_b64 exec, -1
	s_branch .Lc0_end

.Lc0_slow0:
	s_sleep 1
	ds_read_b32 v37, v36 offset:4
	ds_read_b32 v38, v36 offset:68
	s_waitcnt lgkmcnt(0)
	v_readfirstlane_b32 s4, v37
	v_readfirstlane_b32 s5, v38
	s_and_b32 s4, s4, s5
	s_cbranch_scc1 .Lc0_back0
	s_add_i32 s73, s73, 1
	s_cmp_lt_u32 s73, 0x4000
	s_cbranch_scc1 .Lc0_slow0
	s_branch .Lc0_back0
.Lc0_slow1:
	s_sleep 1
	ds_read_b32 v37, v36 offset:8
	ds_read_b32 v38, v36 offset:72
	s_waitcnt lgkmcnt(0)
	v_readfirstlane_b32 s4, v37
	v_readfirstlane_b32 s5, v38
	s_and_b32 s4, s4, s5
	s_cbranch_scc1 .Lc0_back1
	s_add_i32 s73, s73, 1
	s_cmp_lt_u32 s73, 0x4000
	s_cbranch_scc1 .Lc0_slow1
	s_branch .Lc0_back1
.Lc_par1:
	ds_read2_b64 v[48:51], v32 offset0:0 offset1:202
	ds_read_b128 v[120:123], v33 offset:0
	ds_read2_b64 v[10:13], v34 offset0:0 offset1:202
	ds_read2_b64 v[52:55], v32 offset0:1 offset1:203
	ds_read2_b64 v[56:59], v32 offset0:2 offset1:204
	ds_read_b128 v[124:127], v33 offset:16
	ds_read2_b64 v[60:63], v32 offset0:3 offset1:205
	ds_read2_b64 v[64:67], v32 offset0:4 offset1:206
	ds_read_b128 v[128:131], v33 offset:32
	ds_read2_b64 v[68:71], v32 offset0:5 offset1:207
	s_mov_b32 s70, 0
	s_mov_b32 s71, 0

.Lc1_back0:
	s_mov_b32 s72, 0
	s_cmp_eq_u32 s70, 0
	s_cbranch_scc1 .Lc1_nd0
	s_cmp_eq_u32 s36, 3
	s_cbranch_scc0 .Lc1_nd0
	s_mov_b32 s72, 1
	ds_read_b32 v45, v36 offset:124
	ds_read_b128 v[112:115], v43 offset:0
	ds_read_b128 v[116:119], v43 offset:1024

.Lc1_back1:
	s_mov_b32 s72, 0
	s_cmp_eq_u32 s36, 2
	s_cbranch_scc0 .Lc1_nd1
	s_mov_b32 s72, 1
	ds_read_b32 v45, v36 offset:128
	ds_read_b128 v[112:115], v43 offset:2048
	ds_read_b128 v[116:119], v43 offset:3072

.Lc1_next1:
	v_add_u32_e32 v32, 0x100, v32
	v_add_u32_e32 v33, 0x100, v33
	v_add_u32_e32 v34, 0x100, v34
	v_add_u32_e32 v36, 8, v36
	v_add_u32_e32 v39, 0x1000, v39
	v_add_u32_e32 v43, 0x1000, v43
	v_add_u32_e32 v35, 0x800, v35
	s_xor_b32 s71, s71, 2
	s_add_i32 s70, s70, 1
	s_cmp_lt_u32 s70, 6
	s_cbranch_scc1 .Lc1_loop
	s_waitcnt lgkmcnt(6)
	v_pk_fma_f16 v6, v2, v120, v121 op_sel:[0,1,1] op_sel_hi:[1,1,1] neg_lo:[1,0,0] neg_hi:[1,0,0]
	v_pk_fma_f16 v7, v3, v120, v121 op_sel:[0,1,1] op_sel_hi:[1,1,1] neg_lo:[1,0,0] neg_hi:[1,0,0]
	v_pk_fma_f16 v8, v4, v120, v121 op_sel:[0,1,1] op_sel_hi:[1,1,1] neg_lo:[1,0,0] neg_hi:[1,0,0]
	v_pk_fma_f16 v9, v5, v120, v121 op_sel:[0,1,1] op_sel_hi:[1,1,1] neg_lo:[1,0,0] neg_hi:[1,0,0]
	v_mfma_f32_16x16x32_f16 v[18:21], v[10:13], v[2:5], 0
	ds_read2_b64 v[72:75], v32 offset0:6 offset1:208
	ds_read_b128 v[132:135], v33 offset:48
	v_pk_fma_f16 v2, v48, v6, v2
	v_pk_fma_f16 v3, v49, v7, v3
	v_pk_fma_f16 v4, v50, v8, v4
	v_pk_fma_f16 v5, v51, v9, v5
	v_cndmask_b32_e64 v29, v29, v25, s[66:67]
	v_cvt_pk_f16_f32 v30, v26, v27
	v_cvt_pk_f16_f32 v31, v28, v29
	ds_write_b16 v39, v30 offset:0
	ds_write_b16_d16_hi v39, v30 offset:64
	ds_write_b16 v39, v31 offset:128
	ds_write_b16_d16_hi v39, v31 offset:192
	s_mov_b64 exec, 1
	ds_add_u32 v36, v44 offset:124
	s_mov_b64 exec, -1
	v_pk_fma_f16 v6, v2, v122, v123 op_sel:[0,1,1] op_sel_hi:[1,1,1] neg_lo:[1,0,0] neg_hi:[1,0,0]
	v_pk_fma_f16 v7, v3, v122, v123 op_sel:[0,1,1] op_sel_hi:[1,1,1] neg_lo:[1,0,0] neg_hi:[1,0,0]
	v_pk_fma_f16 v8, v4, v122, v123 op_sel:[0,1,1] op_sel_hi:[1,1,1] neg_lo:[1,0,0] neg_hi:[1,0,0]
	v_pk_fma_f16 v9, v5, v122, v123 op_sel:[0,1,1] op_sel_hi:[1,1,1] neg_lo:[1,0,0] neg_hi:[1,0,0]
	v_mfma_f32_16x16x32_f16 v[22:25], v[10:13], v[2:5], 0
	ds_read2_b64 v[76:79], v32 offset0:7 offset1:209
	v_pk_fma_f16 v2, v52, v6, v2
	v_pk_fma_f16 v3, v53, v7, v3
	v_pk_fma_f16 v4, v54, v8, v4
	v_pk_fma_f16 v5, v55, v9, v5
	v_cndmask_b32_e64 v26, v26, v18, s[60:61]
	s_waitcnt lgkmcnt(11)
	v_pk_fma_f16 v6, v2, v124, v125 op_sel:[0,1,1] op_sel_hi:[1,1,1] neg_lo:[1,0,0] neg_hi:[1,0,0]
	v_pk_fma_f16 v7, v3, v124, v125 op_sel:[0,1,1] op_sel_hi:[1,1,1] neg_lo:[1,0,0] neg_hi:[1,0,0]
	v_pk_fma_f16 v8, v4, v124, v125 op_sel:[0,1,1] op_sel_hi:[1,1,1] neg_lo:[1,0,0] neg_hi:[1,0,0]
	v_pk_fma_f16 v9, v5, v124, v125 op_sel:[0,1,1] op_sel_hi:[1,1,1] neg_lo:[1,0,0] neg_hi:[1,0,0]
	v_mfma_f32_16x16x32_f16 v[18:21], v[10:13], v[2:5], 0
	v_pk_fma_f16 v2, v56, v6, v2
	v_pk_fma_f16 v3, v57, v7, v3
	v_pk_fma_f16 v4, v58, v8, v4
	v_pk_fma_f16 v5, v59, v9, v5
	v_cndmask_b32_e64 v27, v27, v23, s[60:61]
	v_pk_fma_f16 v6, v2, v126, v127 op_sel:[0,1,1] op_sel_hi:[1,1,1] neg_lo:[1,0,0] neg_hi:[1,0,0]
	v_pk_fma_f16 v7, v3, v126, v127 op_sel:[0,1,1] op_sel_hi:[1,1,1] neg_lo:[1,0,0] neg_hi:[1,0,0]
	v_pk_fma_f16 v8, v4, v126, v127 op_sel:[0,1,1] op_sel_hi:[1,1,1] neg_lo:[1,0,0] neg_hi:[1,0,0]
	v_pk_fma_f16 v9, v5, v126, v127 op_sel:[0,1,1] op_sel_hi:[1,1,1] neg_lo:[1,0,0] neg_hi:[1,0,0]
	v_mfma_f32_16x16x32_f16 v[22:25], v[10:13], v[2:5], 0
	v_pk_fma_f16 v2, v60, v6, v2
	v_pk_fma_f16 v3, v61, v7, v3
	v_pk_fma_f16 v4, v62, v8, v4
	v_pk_fma_f16 v5, v63, v9, v5
	v_cndmask_b32_e64 v28, v28, v20, s[60:61]
	s_waitcnt lgkmcnt(8)
	s_mov_b32 s72, 0
	s_cmp_eq_u32 s70, 0
	s_cbranch_scc1 .Lc1_ndt
	s_cmp_eq_u32 s36, 3
	s_cbranch_scc0 .Lc1_ndt
	s_mov_b32 s72, 1
	ds_read_b32 v45, v36 offset:124
	ds_read_b128 v[112:115], v43 offset:0
	ds_read_b128 v[116:119], v43 offset:1024

.Lc1_nst:
	v_pk_fma_f16 v6, v2, v134, v135 op_sel:[0,1,1] op_sel_hi:[1,1,1] neg_lo:[1,0,0] neg_hi:[1,0,0]
	v_pk_fma_f16 v7, v3, v134, v135 op_sel:[0,1,1] op_sel_hi:[1,1,1] neg_lo:[1,0,0] neg_hi:[1,0,0]
	v_pk_fma_f16 v8, v4, v134, v135 op_sel:[0,1,1] op_sel_hi:[1,1,1] neg_lo:[1,0,0] neg_hi:[1,0,0]
	v_pk_fma_f16 v9, v5, v134, v135 op_sel:[0,1,1] op_sel_hi:[1,1,1] neg_lo:[1,0,0] neg_hi:[1,0,0]
	v_mfma_f32_16x16x32_f16 v[22:25], v[10:13], v[2:5], 0
	v_pk_fma_f16 v2, v76, v6, v2
	v_pk_fma_f16 v3, v77, v7, v3
	v_pk_fma_f16 v4, v78, v8, v4
	v_pk_fma_f16 v5, v79, v9, v5
	v_cndmask_b32_e64 v28, v28, v20, s[62:63]
	s_nop 7
	v_cndmask_b32_e64 v29, v29, v25, s[62:63]
	v_cvt_pk_f16_f32 v30, v26, v27
	v_cvt_pk_f16_f32 v31, v28, v29
	ds_write_b16 v39, v30 offset:2048
	ds_write_b16_d16_hi v39, v30 offset:2112
	ds_write_b16 v39, v31 offset:2176
	ds_write_b16_d16_hi v39, v31 offset:2240
	s_mov_b64 exec, 1
	ds_add_u32 v36, v44 offset:128
	s_mov_b64 exec, -1
	s_cmp_eq_u32 s36, 2
	s_cbranch_scc0 .Lc1_end
